# pssink2
# speedup vs baseline: 1.0066x; 1.0005x over previous
.LBB3_41:
	ds_read_b64_tr_b16 v[234:235], v213 offset:0x4000
	ds_read_b64_tr_b16 v[236:237], v213 offset:0x4800
	ds_read_b64_tr_b16 v[238:239], v213 offset:0x5000
	ds_read_b64_tr_b16 v[240:241], v213 offset:0x5800
	ds_read_b64_tr_b16 v[242:243], v213 offset:0x6000
	ds_read_b64_tr_b16 v[244:245], v213 offset:0x6800
	ds_read_b64_tr_b16 v[246:247], v213 offset:0x7000
	ds_read_b64_tr_b16 v[248:249], v213 offset:0x7800
	s_add_i32 s6, s60, 64
	s_add_i32 s61, s60, 1
	s_waitcnt lgkmcnt(6)
	v_mfma_f32_32x32x16_bf16 v[64:79], v[180:183], v[234:237], v[64:79]
	ds_read_b64_tr_b16 v[234:235], v213 offset:0x4200
	ds_read_b64_tr_b16 v[236:237], v213 offset:0x4a00
	s_waitcnt lgkmcnt(6)
	v_mfma_f32_32x32x16_bf16 v[64:79], v[184:187], v[238:241], v[64:79]
	ds_read_b64_tr_b16 v[238:239], v213 offset:0x5200
	ds_read_b64_tr_b16 v[240:241], v213 offset:0x5a00
	s_waitcnt lgkmcnt(6)
	v_mfma_f32_32x32x16_bf16 v[64:79], v[188:191], v[242:245], v[64:79]
	ds_read_b64_tr_b16 v[242:243], v213 offset:0x6200
	ds_read_b64_tr_b16 v[244:245], v213 offset:0x6a00
	ds_read_b64_tr_b16 v[250:251], v213 offset:0x7200
	ds_read_b64_tr_b16 v[252:253], v213 offset:0x7a00
	s_waitcnt lgkmcnt(8)
	v_mfma_f32_32x32x16_bf16 v[64:79], v[192:195], v[246:249], v[64:79]
	s_waitcnt lgkmcnt(6)
	v_mfma_f32_32x32x16_bf16 v[48:63], v[180:183], v[234:237], v[48:63]
	ds_read_b64_tr_b16 v[234:235], v213 offset:0x4400
	ds_read_b64_tr_b16 v[236:237], v213 offset:0x4c00
	s_waitcnt lgkmcnt(6)
	v_mfma_f32_32x32x16_bf16 v[48:63], v[184:187], v[238:241], v[48:63]
	ds_read_b64_tr_b16 v[238:239], v213 offset:0x5400
	ds_read_b64_tr_b16 v[240:241], v213 offset:0x5c00
	s_waitcnt lgkmcnt(6)
	v_mfma_f32_32x32x16_bf16 v[48:63], v[188:191], v[242:245], v[48:63]
	ds_read_b64_tr_b16 v[242:243], v213 offset:0x6400
	ds_read_b64_tr_b16 v[244:245], v213 offset:0x6c00
	ds_read_b64_tr_b16 v[246:247], v213 offset:0x7400
	ds_read_b64_tr_b16 v[248:249], v213 offset:0x7c00
	s_waitcnt lgkmcnt(8)
	v_mfma_f32_32x32x16_bf16 v[48:63], v[192:195], v[250:253], v[48:63]
	s_cmp_le_i32 s6, s55
	s_cselect_b64 s[6:7], -1, 0
	s_cmp_gt_i32 s61, s56
	s_cselect_b64 s[62:63], -1, 0
	s_and_b64 s[6:7], s[6:7], s[62:63]
	s_and_b64 vcc, exec, s[6:7]
	s_cbranch_vccnz .LBB3_43
	v_add_u32_e32 v219, 59, v0
	v_cmp_ge_i32_e64 s[64:65], v219, 0
	v_cmp_ge_i32_e64 s[66:67], v219, 32
	v_cmp_ge_i32_e64 s[68:69], v219, 1
	v_cmp_ge_i32_e64 s[70:71], v219, 33
	v_cmp_ge_i32_e64 s[72:73], v219, 2
	v_cmp_ge_i32_e64 s[74:75], v219, 34
	v_cmp_ge_i32_e64 s[76:77], v219, 3
	v_cmp_ge_i32_e64 s[78:79], v219, 35
	v_cndmask_b32_e64 v128, v221, v128, s[64:65]
	v_cndmask_b32_e64 v112, v221, v112, s[66:67]
	v_cndmask_b32_e64 v129, v221, v129, s[68:69]
	v_cndmask_b32_e64 v113, v221, v113, s[70:71]
	v_cndmask_b32_e64 v130, v221, v130, s[72:73]
	v_cndmask_b32_e64 v114, v221, v114, s[74:75]
	v_cndmask_b32_e64 v131, v221, v131, s[76:77]
	v_cndmask_b32_e64 v115, v221, v115, s[78:79]
	v_cmp_ge_i32_e64 s[64:65], v219, 8
	v_cmp_ge_i32_e64 s[66:67], v219, 40
	v_cmp_ge_i32_e64 s[68:69], v219, 9
	v_cmp_ge_i32_e64 s[70:71], v219, 41
	v_cmp_ge_i32_e64 s[72:73], v219, 10
	v_cmp_ge_i32_e64 s[74:75], v219, 42
	v_cmp_ge_i32_e64 s[76:77], v219, 11
	v_cmp_ge_i32_e64 s[78:79], v219, 43
	v_cndmask_b32_e64 v132, v221, v132, s[64:65]
	v_cndmask_b32_e64 v116, v221, v116, s[66:67]
	v_cndmask_b32_e64 v133, v221, v133, s[68:69]
	v_cndmask_b32_e64 v117, v221, v117, s[70:71]
	v_cndmask_b32_e64 v134, v221, v134, s[72:73]
	v_cndmask_b32_e64 v118, v221, v118, s[74:75]
	v_cndmask_b32_e64 v135, v221, v135, s[76:77]
	v_cndmask_b32_e64 v119, v221, v119, s[78:79]
	v_cmp_ge_i32_e64 s[64:65], v219, 16
	v_cmp_ge_i32_e64 s[66:67], v219, 48
	v_cmp_ge_i32_e64 s[68:69], v219, 17
	v_cmp_ge_i32_e64 s[70:71], v219, 49
	v_cmp_ge_i32_e64 s[72:73], v219, 18
	v_cmp_ge_i32_e64 s[74:75], v219, 50
	v_cmp_ge_i32_e64 s[76:77], v219, 19
	v_cmp_ge_i32_e64 s[78:79], v219, 51
	v_cndmask_b32_e64 v136, v221, v136, s[64:65]
	v_cndmask_b32_e64 v120, v221, v120, s[66:67]
	v_cndmask_b32_e64 v137, v221, v137, s[68:69]
	v_cndmask_b32_e64 v121, v221, v121, s[70:71]
	v_cndmask_b32_e64 v138, v221, v138, s[72:73]
	v_cndmask_b32_e64 v122, v221, v122, s[74:75]
	v_cndmask_b32_e64 v139, v221, v139, s[76:77]
	v_cndmask_b32_e64 v123, v221, v123, s[78:79]
	v_cmp_ge_i32_e64 s[64:65], v219, 24
	v_cmp_ge_i32_e64 s[66:67], v219, 56
	v_cmp_ge_i32_e64 s[68:69], v219, 25
	v_cmp_ge_i32_e64 s[70:71], v219, 57
	v_cmp_ge_i32_e64 s[72:73], v219, 26
	v_cmp_ge_i32_e64 s[74:75], v219, 58
	v_cmp_ge_i32_e64 s[76:77], v219, 27
	v_cmp_ge_i32_e64 s[78:79], v219, 59
	v_cndmask_b32_e64 v140, v221, v140, s[64:65]
	v_cndmask_b32_e64 v124, v221, v124, s[66:67]
	v_cndmask_b32_e64 v141, v221, v141, s[68:69]
	v_cndmask_b32_e64 v125, v221, v125, s[70:71]
	v_cndmask_b32_e64 v142, v221, v142, s[72:73]
	v_cndmask_b32_e64 v126, v221, v126, s[74:75]
	v_cndmask_b32_e64 v143, v221, v143, s[76:77]
	v_cndmask_b32_e64 v127, v221, v127, s[78:79]
.LBB3_43:
	s_waitcnt lgkmcnt(6)
	v_mfma_f32_32x32x16_bf16 v[32:47], v[180:183], v[234:237], v[32:47]
	v_max_f32_e32 v218, v129, v129
	v_max_f32_e32 v219, v128, v128
	v_max_f32_e32 v218, v219, v218
	v_max3_f32 v218, v218, v130, v131
	v_max3_f32 v218, v218, v132, v133
	ds_read_b64_tr_b16 v[234:235], v213 offset:0x4600
	ds_read_b64_tr_b16 v[236:237], v213 offset:0x4e00
	s_waitcnt lgkmcnt(6)
	v_mfma_f32_32x32x16_bf16 v[32:47], v[184:187], v[238:241], v[32:47]
	v_max3_f32 v218, v218, v134, v135
	v_max3_f32 v218, v218, v136, v137
	v_max3_f32 v218, v218, v138, v139
	v_max3_f32 v218, v218, v140, v141
	v_max3_f32 v218, v218, v142, v143
	ds_read_b64_tr_b16 v[238:239], v213 offset:0x5600
	ds_read_b64_tr_b16 v[240:241], v213 offset:0x5e00
	s_waitcnt lgkmcnt(6)
	v_mfma_f32_32x32x16_bf16 v[32:47], v[188:191], v[242:245], v[32:47]
	v_max3_f32 v218, v218, v112, v113
	v_max3_f32 v218, v218, v114, v115
	v_max3_f32 v218, v218, v116, v117
	v_max3_f32 v218, v218, v118, v119
	v_max3_f32 v218, v218, v120, v121
	ds_read_b64_tr_b16 v[242:243], v213 offset:0x6600
	ds_read_b64_tr_b16 v[244:245], v213 offset:0x6e00
	ds_read_b64_tr_b16 v[250:251], v213 offset:0x7600
	ds_read_b64_tr_b16 v[252:253], v213 offset:0x7e00
	s_waitcnt lgkmcnt(8)
	v_mfma_f32_32x32x16_bf16 v[32:47], v[192:195], v[246:249], v[32:47]
	v_max3_f32 v218, v218, v122, v123
	v_max3_f32 v218, v218, v124, v125
	v_max3_f32 v218, v218, v126, v127
	v_mov_b32_e32 v219, v218
	s_nop 1
	v_permlane32_swap_b32_e32 v218, v219
	s_waitcnt lgkmcnt(6)
	v_mfma_f32_32x32x16_bf16 v[16:31], v[180:183], v[234:237], v[16:31]
	v_max_f32_e32 v219, v219, v219
	v_max_f32_e32 v218, v218, v218
	v_max_f32_e32 v218, v218, v219
	v_sub_f32_e32 v219, v218, v231
	v_mul_f32_e32 v219, 0x3db504f3, v219
	s_waitcnt lgkmcnt(4)
	v_mfma_f32_32x32x16_bf16 v[16:31], v[184:187], v[238:241], v[16:31]
	s_waitcnt lgkmcnt(2)
	v_mfma_f32_32x32x16_bf16 v[16:31], v[188:191], v[242:245], v[16:31]
	s_waitcnt lgkmcnt(0)
	v_mfma_f32_32x32x16_bf16 v[16:31], v[192:195], v[250:253], v[16:31]
	v_cmp_ge_f32_e32 vcc, s20, v219
	s_cmp_eq_u64 vcc, exec
	s_cselect_b64 s[6:7], -1, 0
	s_andn2_b64 vcc, exec, s[46:47]
	s_barrier
	s_cbranch_vccnz .LBB3_45
	s_waitcnt vmcnt(0)
	s_waitcnt vmcnt(3)
	ds_write_b128 v215, v[2:5] offset:16384
	s_waitcnt vmcnt(2)
	ds_write_b128 v216, v[6:9] offset:16384
	s_waitcnt vmcnt(1)
	ds_write_b128 v222, v[10:13] offset:50176
	s_waitcnt vmcnt(0)
	ds_write_b128 v222, v[176:179] offset:58880
.LBB3_45:
	s_waitcnt vmcnt(3)
	v_max_f32_e32 v2, v231, v231
	v_max_f32_e32 v3, v2, v218
	v_sub_f32_e32 v2, v231, v3
	v_mul_f32_e32 v2, 0x3e0293ee, v2
	v_exp_f32_e32 v2, v2
	s_nop 0
	v_cndmask_b32_e64 v2, v2, 1.0, s[6:7]
	v_cmp_gt_f32_e32 vcc, 1.0, v2
	s_cbranch_vccz .LBB3_32
	s_and_saveexec_b64 s[46:47], s[0:1]
	s_cbranch_execz .LBB3_31
	ds_write_b32 v226, v2 offset:128
	s_branch .LBB3_31
